# P2 in-proj epilogue: permlane16 swaps + 16 dwordx4 stores (64 contiguous bytes per row) instead of 32 dwordx2
# speedup vs baseline: 1.0295x; 1.0072x over previous
.LBB0_154:
	v_add_u32_e32 v130, s27, v212
	v_ashrrev_i32_e32 v131, 31, v130
	s_ashr_i32 s27, s26, 31
	v_lshlrev_b64 v[252:253], 13, v[130:131]
	s_lshl_b64 s[6:7], s[26:27], 1
	v_bfe_u32 v251, v178, 4, 1
	v_bfe_u32 v254, v178, 5, 1
	v_lshlrev_b32_e32 v251, 5, v251
	v_lshl_add_u32 v254, v254, 4, v251
	v_mov_b32_e32 v255, 0
	v_lshl_add_u64 v[252:253], s[16:17], 0, v[252:253]
	v_lshl_add_u64 v[252:253], v[252:253], 0, s[6:7]
	v_lshl_add_u64 v[252:253], v[252:253], 0, s[18:19]
	v_lshl_add_u64 v[252:253], v[252:253], 0, v[254:255]
	s_mov_b64 s[100:101], 0x20000
	v_cvt_pk_bf16_f32 v126, v126, v127
	v_cvt_pk_bf16_f32 v127, v128, v129
	v_cvt_pk_bf16_f32 v128, v122, v123
	v_cvt_pk_bf16_f32 v129, v124, v125
	v_cvt_pk_bf16_f32 v114, v114, v115
	v_cvt_pk_bf16_f32 v115, v116, v117
	v_cvt_pk_bf16_f32 v116, v106, v107
	v_cvt_pk_bf16_f32 v117, v108, v109
	s_nop 1
	v_permlane16_swap_b32_e32 v126, v128
	v_permlane16_swap_b32_e32 v127, v129
	v_permlane16_swap_b32_e32 v114, v116
	v_permlane16_swap_b32_e32 v115, v117
	global_store_dwordx4 v[252:253], v[126:129], off
	global_store_dwordx4 v[252:253], v[114:117], off offset:256
	v_lshl_add_u64 v[252:253], v[252:253], 0, s[100:101]
	v_cvt_pk_bf16_f32 v118, v118, v119
	v_cvt_pk_bf16_f32 v119, v120, v121
	v_cvt_pk_bf16_f32 v120, v110, v111
	v_cvt_pk_bf16_f32 v121, v112, v113
	v_cvt_pk_bf16_f32 v98, v98, v99
	v_cvt_pk_bf16_f32 v99, v100, v101
	v_cvt_pk_bf16_f32 v100, v90, v91
	v_cvt_pk_bf16_f32 v101, v92, v93
	s_nop 1
	v_permlane16_swap_b32_e32 v118, v120
	v_permlane16_swap_b32_e32 v119, v121
	v_permlane16_swap_b32_e32 v98, v100
	v_permlane16_swap_b32_e32 v99, v101
	global_store_dwordx4 v[252:253], v[118:121], off
	global_store_dwordx4 v[252:253], v[98:101], off offset:256
	v_lshl_add_u64 v[252:253], v[252:253], 0, s[100:101]
	v_cvt_pk_bf16_f32 v102, v102, v103
	v_cvt_pk_bf16_f32 v103, v104, v105
	v_cvt_pk_bf16_f32 v104, v94, v95
	v_cvt_pk_bf16_f32 v105, v96, v97
	v_cvt_pk_bf16_f32 v82, v82, v83
	v_cvt_pk_bf16_f32 v83, v84, v85
	v_cvt_pk_bf16_f32 v84, v74, v75
	v_cvt_pk_bf16_f32 v85, v76, v77
	s_nop 1
	v_permlane16_swap_b32_e32 v102, v104
	v_permlane16_swap_b32_e32 v103, v105
	v_permlane16_swap_b32_e32 v82, v84
	v_permlane16_swap_b32_e32 v83, v85
	global_store_dwordx4 v[252:253], v[102:105], off
	global_store_dwordx4 v[252:253], v[82:85], off offset:256
	v_lshl_add_u64 v[252:253], v[252:253], 0, s[100:101]
	v_cvt_pk_bf16_f32 v86, v86, v87
	v_cvt_pk_bf16_f32 v87, v88, v89
	v_cvt_pk_bf16_f32 v88, v78, v79
	v_cvt_pk_bf16_f32 v89, v80, v81
	v_cvt_pk_bf16_f32 v70, v70, v71
	v_cvt_pk_bf16_f32 v71, v72, v73
	v_cvt_pk_bf16_f32 v72, v66, v67
	v_cvt_pk_bf16_f32 v73, v68, v69
	s_nop 1
	v_permlane16_swap_b32_e32 v86, v88
	v_permlane16_swap_b32_e32 v87, v89
	v_permlane16_swap_b32_e32 v70, v72
	v_permlane16_swap_b32_e32 v71, v73
	global_store_dwordx4 v[252:253], v[86:89], off
	global_store_dwordx4 v[252:253], v[70:73], off offset:256
	s_mov_b64 s[100:101], 0xa0000
	v_lshl_add_u64 v[252:253], v[252:253], 0, s[100:101]
	s_mov_b64 s[100:101], 0x20000
	v_cvt_pk_bf16_f32 v62, v62, v63
	v_cvt_pk_bf16_f32 v63, v64, v65
	v_cvt_pk_bf16_f32 v64, v58, v59
	v_cvt_pk_bf16_f32 v65, v60, v61
	v_cvt_pk_bf16_f32 v50, v50, v51
	v_cvt_pk_bf16_f32 v51, v52, v53
	v_cvt_pk_bf16_f32 v52, v42, v43
	v_cvt_pk_bf16_f32 v53, v44, v45
	s_nop 1
	v_permlane16_swap_b32_e32 v62, v64
	v_permlane16_swap_b32_e32 v63, v65
	v_permlane16_swap_b32_e32 v50, v52
	v_permlane16_swap_b32_e32 v51, v53
	global_store_dwordx4 v[252:253], v[62:65], off
	global_store_dwordx4 v[252:253], v[50:53], off offset:256
	v_lshl_add_u64 v[252:253], v[252:253], 0, s[100:101]
	v_cvt_pk_bf16_f32 v54, v54, v55
	v_cvt_pk_bf16_f32 v55, v56, v57
	v_cvt_pk_bf16_f32 v56, v46, v47
	v_cvt_pk_bf16_f32 v57, v48, v49
	v_cvt_pk_bf16_f32 v34, v34, v35
	v_cvt_pk_bf16_f32 v35, v36, v37
	v_cvt_pk_bf16_f32 v36, v26, v27
	v_cvt_pk_bf16_f32 v37, v28, v29
	s_nop 1
	v_permlane16_swap_b32_e32 v54, v56
	v_permlane16_swap_b32_e32 v55, v57
	v_permlane16_swap_b32_e32 v34, v36
	v_permlane16_swap_b32_e32 v35, v37
	global_store_dwordx4 v[252:253], v[54:57], off
	global_store_dwordx4 v[252:253], v[34:37], off offset:256
	v_lshl_add_u64 v[252:253], v[252:253], 0, s[100:101]
	v_cvt_pk_bf16_f32 v38, v38, v39
	v_cvt_pk_bf16_f32 v39, v40, v41
	v_cvt_pk_bf16_f32 v40, v30, v31
	v_cvt_pk_bf16_f32 v41, v32, v33
	v_cvt_pk_bf16_f32 v18, v18, v19
	v_cvt_pk_bf16_f32 v19, v20, v21
	v_cvt_pk_bf16_f32 v20, v10, v11
	v_cvt_pk_bf16_f32 v21, v12, v13
	s_nop 1
	v_permlane16_swap_b32_e32 v38, v40
	v_permlane16_swap_b32_e32 v39, v41
	v_permlane16_swap_b32_e32 v18, v20
	v_permlane16_swap_b32_e32 v19, v21
	global_store_dwordx4 v[252:253], v[38:41], off
	global_store_dwordx4 v[252:253], v[18:21], off offset:256
	v_lshl_add_u64 v[252:253], v[252:253], 0, s[100:101]
	v_cvt_pk_bf16_f32 v22, v22, v23
	v_cvt_pk_bf16_f32 v23, v24, v25
	v_cvt_pk_bf16_f32 v24, v14, v15
	v_cvt_pk_bf16_f32 v25, v16, v17
	v_cvt_pk_bf16_f32 v6, v6, v7
	v_cvt_pk_bf16_f32 v7, v8, v9
	v_cvt_pk_bf16_f32 v8, v2, v3
	v_cvt_pk_bf16_f32 v9, v4, v5
	s_nop 1
	v_permlane16_swap_b32_e32 v22, v24
	v_permlane16_swap_b32_e32 v23, v25
	v_permlane16_swap_b32_e32 v6, v8
	v_permlane16_swap_b32_e32 v7, v9
	global_store_dwordx4 v[252:253], v[22:25], off
	global_store_dwordx4 v[252:253], v[6:9], off offset:256
	s_and_b64 vcc, exec, s[4:5]
	s_mov_b32 s34, s58
	s_mov_b64 s[28:29], s[24:25]
	s_mov_b32 s27, s59
	s_mov_b32 s26, s57
	s_cbranch_vccnz .LBB0_168
